# combine phase: a token's 24 row-piece loads in flight together; prologue x->bf16/fp8: 8 loads in flight + hardware RNE bf16 pack
# baseline (speedup 1.0000x reference)
.LBB0_911:
	s_mov_b32 s4, 0
	s_ashr_i32 s5, s4, 31
	s_lshl_b64 s[4:5], s[4:5], 3
	s_add_u32 s4, s92, s4
	s_addc_u32 s5, s93, s5
	s_load_dwordx2 s[4:5], s[4:5], 0x0
	s_waitcnt lgkmcnt(0)
	v_lshl_add_u64 v[8:9], s[6:7], 0, v[4:5]
	v_lshl_add_u64 v[42:43], s[4:5], 0, v[2:3]
	global_load_dwordx4 v[14:17], v[42:43], off offset:-4096
	global_load_dwordx4 v[18:21], v[42:43], off offset:-3072
	global_load_dwordx4 v[22:25], v[42:43], off offset:-2048
	global_load_dwordx4 v[26:29], v[42:43], off offset:-1024
	global_load_dwordx4 v[30:33], v[42:43], off
	global_load_dwordx4 v[34:37], v[42:43], off offset:1024
	global_load_dwordx4 v[38:41], v[42:43], off offset:2048
	s_nop 0
	global_load_dwordx4 v[42:45], v[42:43], off offset:3072
	v_add_co_u32_e64 v8, s[4:5], s9, v8
	v_lshl_add_u64 v[10:11], s[6:7], 0, v[6:7]
	s_nop 0
	v_addc_co_u32_e64 v9, s[4:5], 0, v9, s[4:5]
	v_add_co_u32_e64 v10, s[4:5], s11, v10
	s_nop 1
	v_addc_co_u32_e64 v11, s[4:5], 0, v11, s[4:5]
	s_waitcnt vmcnt(7)
	v_mul_f32_e32 v46, v15, v15
	v_mul_f32_e32 v13, v17, v17
	v_fmac_f32_e32 v46, v14, v14
	v_fmac_f32_e32 v13, v16, v16
	v_add_f32_e32 v46, v46, v13
	v_cvt_pk_fp8_f32 v13, v14, v15
	v_cvt_pk_fp8_f32 v13, v16, v17 op_sel:[0,0,1]
	global_store_dword v[10:11], v13, off
	v_cvt_pk_bf16_f32 v14, v14, v15
	v_cvt_pk_bf16_f32 v15, v16, v17
	global_store_dwordx2 v[8:9], v[14:15], off
	s_waitcnt vmcnt(8)
	v_mul_f32_e32 v13, v19, v19
	v_mul_f32_e32 v16, v21, v21
	v_fmac_f32_e32 v13, v18, v18
	v_fmac_f32_e32 v16, v20, v20
	v_add_f32_e32 v13, v13, v16
	v_add_f32_e32 v46, v46, v13
	v_cvt_pk_fp8_f32 v13, v18, v19
	v_cvt_pk_fp8_f32 v13, v20, v21 op_sel:[0,0,1]
	global_store_dword v[10:11], v13, off offset:256
	v_cvt_pk_bf16_f32 v18, v18, v19
	v_cvt_pk_bf16_f32 v19, v20, v21
	global_store_dwordx2 v[8:9], v[18:19], off offset:512
	s_waitcnt vmcnt(9)
	v_mul_f32_e32 v13, v23, v23
	v_mul_f32_e32 v20, v25, v25
	v_fmac_f32_e32 v13, v22, v22
	v_fmac_f32_e32 v20, v24, v24
	v_add_f32_e32 v13, v13, v20
	v_add_f32_e32 v46, v46, v13
	v_cvt_pk_fp8_f32 v13, v22, v23
	v_cvt_pk_fp8_f32 v13, v24, v25 op_sel:[0,0,1]
	global_store_dword v[10:11], v13, off offset:512
	v_cvt_pk_bf16_f32 v22, v22, v23
	v_cvt_pk_bf16_f32 v23, v24, v25
	global_store_dwordx2 v[8:9], v[22:23], off offset:1024
	s_waitcnt vmcnt(10)
	v_mul_f32_e32 v13, v27, v27
	v_mul_f32_e32 v24, v29, v29
	v_fmac_f32_e32 v13, v26, v26
	v_fmac_f32_e32 v24, v28, v28
	v_add_f32_e32 v13, v13, v24
	v_add_f32_e32 v46, v46, v13
	v_cvt_pk_fp8_f32 v13, v26, v27
	v_cvt_pk_fp8_f32 v13, v28, v29 op_sel:[0,0,1]
	global_store_dword v[10:11], v13, off offset:768
	v_cvt_pk_bf16_f32 v26, v26, v27
	v_cvt_pk_bf16_f32 v27, v28, v29
	global_store_dwordx2 v[8:9], v[26:27], off offset:1536
	s_waitcnt vmcnt(11)
	v_mul_f32_e32 v13, v31, v31
	v_mul_f32_e32 v28, v33, v33
	v_fmac_f32_e32 v13, v30, v30
	v_fmac_f32_e32 v28, v32, v32
	v_add_f32_e32 v13, v13, v28
	v_add_f32_e32 v46, v46, v13
	v_cvt_pk_fp8_f32 v13, v30, v31
	v_cvt_pk_fp8_f32 v13, v32, v33 op_sel:[0,0,1]
	global_store_dword v[10:11], v13, off offset:1024
	v_cvt_pk_bf16_f32 v30, v30, v31
	v_cvt_pk_bf16_f32 v31, v32, v33
	global_store_dwordx2 v[8:9], v[30:31], off offset:2048
	s_waitcnt vmcnt(12)
	v_mul_f32_e32 v13, v35, v35
	v_mul_f32_e32 v32, v37, v37
	v_fmac_f32_e32 v13, v34, v34
	v_fmac_f32_e32 v32, v36, v36
	v_add_f32_e32 v13, v13, v32
	v_add_f32_e32 v46, v46, v13
	v_cvt_pk_fp8_f32 v13, v34, v35
	v_cvt_pk_fp8_f32 v13, v36, v37 op_sel:[0,0,1]
	global_store_dword v[10:11], v13, off offset:1280
	v_cvt_pk_bf16_f32 v34, v34, v35
	v_cvt_pk_bf16_f32 v35, v36, v37
	global_store_dwordx2 v[8:9], v[34:35], off offset:2560
	s_waitcnt vmcnt(13)
	v_mul_f32_e32 v13, v39, v39
	v_mul_f32_e32 v36, v41, v41
	v_fmac_f32_e32 v13, v38, v38
	v_fmac_f32_e32 v36, v40, v40
	v_add_f32_e32 v13, v13, v36
	v_add_f32_e32 v46, v46, v13
	v_cvt_pk_fp8_f32 v13, v38, v39
	v_cvt_pk_fp8_f32 v13, v40, v41 op_sel:[0,0,1]
	global_store_dword v[10:11], v13, off offset:1536
	v_cvt_pk_bf16_f32 v38, v38, v39
	v_cvt_pk_bf16_f32 v39, v40, v41
	global_store_dwordx2 v[8:9], v[38:39], off offset:3072
	s_waitcnt vmcnt(14)
	v_mul_f32_e32 v13, v43, v43
	v_mul_f32_e32 v40, v45, v45
	v_fmac_f32_e32 v13, v42, v42
	v_fmac_f32_e32 v40, v44, v44
	v_add_f32_e32 v13, v13, v40
	v_add_f32_e32 v46, v46, v13
	v_cvt_pk_fp8_f32 v13, v42, v43
	v_cvt_pk_fp8_f32 v13, v44, v45 op_sel:[0,0,1]
	global_store_dword v[10:11], v13, off offset:1792
	v_cvt_pk_bf16_f32 v42, v42, v43
	v_cvt_pk_bf16_f32 v43, v44, v45
	global_store_dwordx2 v[8:9], v[42:43], off offset:3584
	v_mov_b32_e32 v9, v46
	v_mbcnt_lo_u32_b32 v8, -1, 0
	v_mbcnt_hi_u32_b32 v8, -1, v8
	v_mbcnt_lo_u32_b32 v10, -1, 0
	v_mbcnt_hi_u32_b32 v10, -1, v10
	s_nop 0
	v_lshlrev_b32_e32 v8, 2, v8
	v_xor_b32_e32 v8, 4, v8
	ds_bpermute_b32 v8, v8, v9
	v_lshlrev_b32_e32 v10, 2, v10
	v_xor_b32_e32 v10, 8, v10
	s_waitcnt lgkmcnt(0)
	v_add_f32_e32 v8, v9, v8
	ds_bpermute_b32 v9, v10, v8
	v_mbcnt_lo_u32_b32 v10, -1, 0
	v_mbcnt_hi_u32_b32 v10, -1, v10
	s_waitcnt lgkmcnt(0)
	v_add_f32_e32 v8, v8, v9
	v_lshlrev_b32_e32 v10, 2, v10
	v_xor_b32_e32 v10, 16, v10
	ds_bpermute_b32 v9, v10, v8
	v_mbcnt_lo_u32_b32 v10, -1, 0
	v_mbcnt_hi_u32_b32 v10, -1, v10
	s_waitcnt lgkmcnt(0)
	v_add_f32_e32 v8, v8, v9
	v_lshlrev_b32_e32 v10, 2, v10
	v_xor_b32_e32 v10, 32, v10
	ds_bpermute_b32 v9, v10, v8
	v_mbcnt_lo_u32_b32 v10, -1, 0
	v_mbcnt_hi_u32_b32 v10, -1, v10
	s_waitcnt lgkmcnt(0)
	v_add_f32_e32 v8, v8, v9
	v_lshlrev_b32_e32 v10, 2, v10
	v_xor_b32_e32 v10, 64, v10
	ds_bpermute_b32 v9, v10, v8
	v_mbcnt_lo_u32_b32 v10, -1, 0
	v_mbcnt_hi_u32_b32 v10, -1, v10
	s_waitcnt lgkmcnt(0)
	v_add_f32_e32 v8, v8, v9
	v_lshlrev_b32_e32 v10, 2, v10
	v_xor_b32_e32 v9, 0x80, v10
	ds_bpermute_b32 v9, v9, v8
	s_and_saveexec_b64 s[4:5], vcc
	s_cbranch_execz .LBB0_910
	s_waitcnt lgkmcnt(0)
	v_add_f32_e32 v8, v8, v9
	v_lshl_add_u64 v[10:11], s[6:7], 0, v[0:1]
	v_cndmask_b32_e64 v8, 0, v8, s[2:3]
	global_store_dword v[10:11], v8, off
	s_branch .LBB0_910

.LBB0_1885:
	s_ashr_i32 s9, s8, 31
	s_lshl_b64 s[36:37], s[8:9], 2
	s_add_u32 s38, s31, s36
	s_addc_u32 s39, s33, s37
	global_load_dwordx2 v[12:13], v177, s[38:39]
	global_load_dwordx2 v[26:27], v[2:3], off
	global_load_dwordx2 v[28:29], v[2:3], off offset:512
	global_load_dwordx2 v[30:31], v[2:3], off offset:1024
	global_load_dwordx2 v[32:33], v[2:3], off offset:1536
	global_load_dwordx2 v[34:35], v[2:3], off offset:2048
	global_load_dwordx2 v[36:37], v[2:3], off offset:2560
	global_load_dwordx2 v[38:39], v[2:3], off offset:3072
	global_load_dwordx2 v[40:41], v[2:3], off offset:3584
	s_add_i32 s40, s8, 1
	s_ashr_i32 s41, s40, 31
	s_add_u32 s36, s18, s36
	s_addc_u32 s37, s19, s37
	global_load_dword v6, v177, s[36:37]
	s_lshl_b64 s[38:39], s[40:41], 2
	s_add_u32 s36, s18, s38
	s_addc_u32 s37, s19, s39
	global_load_dword v8, v177, s[36:37]
	v_lshl_add_u64 v[2:3], v[2:3], 0, s[4:5]
	s_waitcnt vmcnt(10)
	v_readfirstlane_b32 s1, v12
	v_readfirstlane_b32 s3, v13
	s_ashr_i32 s9, s1, 14
	s_ashr_i32 s35, s3, 14
	s_cmp_eq_u32 s9, 1
	s_cselect_b32 s36, s20, 0
	s_cmp_eq_u32 s35, 1
	s_cselect_b32 s37, s20, 0
	s_cmp_eq_u32 s9, 2
	s_cselect_b32 s36, s21, s36
	s_cmp_eq_u32 s35, 2
	s_cselect_b32 s37, s21, s37
	s_cmp_eq_u32 s9, 3
	s_cselect_b32 s36, s22, s36
	s_cmp_eq_u32 s35, 3
	s_cselect_b32 s37, s22, s37
	s_cmp_eq_u32 s9, 4
	s_cselect_b32 s36, s23, s36
	s_cmp_eq_u32 s35, 4
	s_cselect_b32 s37, s23, s37
	s_cmp_eq_u32 s9, 5
	s_cselect_b32 s36, s28, s36
	s_cmp_eq_u32 s35, 5
	s_cselect_b32 s37, s28, s37
	s_cmp_eq_u32 s9, 6
	s_cselect_b32 s36, s29, s36
	s_cmp_eq_u32 s35, 6
	s_cselect_b32 s37, s29, s37
	s_cmp_eq_u32 s9, 7
	s_cselect_b32 s9, s30, s36
	s_cmp_eq_u32 s35, 7
	s_cselect_b32 s35, s30, s37
	s_lshl_b32 s9, s9, 8
	s_and_b32 s1, s1, 0x3fff
	s_and_b32 s3, s3, 0x3fff
	s_add_i32 s36, s9, s1
	s_lshl_b32 s1, s35, 8
	s_ashr_i32 s37, s36, 31
	s_add_i32 s38, s1, s3
	s_lshl_b64 s[36:37], s[36:37], 12
	s_ashr_i32 s39, s38, 31
	s_lshl_b64 s[38:39], s[38:39], 12
	v_lshl_add_u64 v[10:11], v[0:1], 0, s[36:37]
	v_lshl_add_u64 v[12:13], v[0:1], 0, s[38:39]
	global_load_dwordx2 v[42:43], v[10:11], off
	global_load_dwordx2 v[58:59], v[12:13], off
	global_load_dwordx2 v[44:45], v[10:11], off offset:512
	global_load_dwordx2 v[60:61], v[12:13], off offset:512
	global_load_dwordx2 v[46:47], v[10:11], off offset:1024
	global_load_dwordx2 v[62:63], v[12:13], off offset:1024
	global_load_dwordx2 v[48:49], v[10:11], off offset:1536
	global_load_dwordx2 v[64:65], v[12:13], off offset:1536
	global_load_dwordx2 v[50:51], v[10:11], off offset:2048
	global_load_dwordx2 v[66:67], v[12:13], off offset:2048
	global_load_dwordx2 v[52:53], v[10:11], off offset:2560
	global_load_dwordx2 v[68:69], v[12:13], off offset:2560
	global_load_dwordx2 v[54:55], v[10:11], off offset:3072
	global_load_dwordx2 v[70:71], v[12:13], off offset:3072
	global_load_dwordx2 v[56:57], v[10:11], off offset:3584
	global_load_dwordx2 v[72:73], v[12:13], off offset:3584
	s_add_i32 s0, s0, s2
	s_add_i32 s8, s8, s34
	s_cmpk_lt_i32 s0, 0x4000
	s_waitcnt vmcnt(14)
	v_lshlrev_b32_e32 v20, 16, v26
	v_and_b32_e32 v21, 0xffff0000, v26
	v_lshlrev_b32_e32 v22, 16, v42
	v_and_b32_e32 v23, 0xffff0000, v42
	v_lshlrev_b32_e32 v14, 16, v27
	v_and_b32_e32 v15, 0xffff0000, v27
	v_lshlrev_b32_e32 v16, 16, v43
	v_and_b32_e32 v17, 0xffff0000, v43
	v_lshlrev_b32_e32 v24, 16, v58
	v_and_b32_e32 v25, 0xffff0000, v58
	v_lshlrev_b32_e32 v18, 16, v59
	v_and_b32_e32 v19, 0xffff0000, v59
	v_pk_fma_f32 v[20:21], v[6:7], v[22:23], v[20:21] op_sel_hi:[0,1,1]
	v_pk_fma_f32 v[14:15], v[6:7], v[16:17], v[14:15] op_sel_hi:[0,1,1]
	v_pk_fma_f32 v[16:17], v[8:9], v[18:19], v[14:15] op_sel_hi:[0,1,1]
	v_pk_fma_f32 v[14:15], v[8:9], v[24:25], v[20:21] op_sel_hi:[0,1,1]
	global_store_dwordx4 v[4:5], v[14:17], off offset:-4096
	s_waitcnt vmcnt(13)
	v_lshlrev_b32_e32 v20, 16, v28
	v_and_b32_e32 v21, 0xffff0000, v28
	v_lshlrev_b32_e32 v22, 16, v44
	v_and_b32_e32 v23, 0xffff0000, v44
	v_lshlrev_b32_e32 v14, 16, v29
	v_and_b32_e32 v15, 0xffff0000, v29
	v_lshlrev_b32_e32 v16, 16, v45
	v_and_b32_e32 v17, 0xffff0000, v45
	v_lshlrev_b32_e32 v24, 16, v60
	v_and_b32_e32 v25, 0xffff0000, v60
	v_lshlrev_b32_e32 v18, 16, v61
	v_and_b32_e32 v19, 0xffff0000, v61
	v_pk_fma_f32 v[20:21], v[6:7], v[22:23], v[20:21] op_sel_hi:[0,1,1]
	v_pk_fma_f32 v[14:15], v[6:7], v[16:17], v[14:15] op_sel_hi:[0,1,1]
	v_pk_fma_f32 v[16:17], v[8:9], v[18:19], v[14:15] op_sel_hi:[0,1,1]
	v_pk_fma_f32 v[14:15], v[8:9], v[24:25], v[20:21] op_sel_hi:[0,1,1]
	global_store_dwordx4 v[4:5], v[14:17], off offset:-3072
	s_waitcnt vmcnt(12)
	v_lshlrev_b32_e32 v20, 16, v30
	v_and_b32_e32 v21, 0xffff0000, v30
	v_lshlrev_b32_e32 v22, 16, v46
	v_and_b32_e32 v23, 0xffff0000, v46
	v_lshlrev_b32_e32 v14, 16, v31
	v_and_b32_e32 v15, 0xffff0000, v31
	v_lshlrev_b32_e32 v16, 16, v47
	v_and_b32_e32 v17, 0xffff0000, v47
	v_lshlrev_b32_e32 v24, 16, v62
	v_and_b32_e32 v25, 0xffff0000, v62
	v_lshlrev_b32_e32 v18, 16, v63
	v_and_b32_e32 v19, 0xffff0000, v63
	v_pk_fma_f32 v[20:21], v[6:7], v[22:23], v[20:21] op_sel_hi:[0,1,1]
	v_pk_fma_f32 v[14:15], v[6:7], v[16:17], v[14:15] op_sel_hi:[0,1,1]
	v_pk_fma_f32 v[16:17], v[8:9], v[18:19], v[14:15] op_sel_hi:[0,1,1]
	v_pk_fma_f32 v[14:15], v[8:9], v[24:25], v[20:21] op_sel_hi:[0,1,1]
	global_store_dwordx4 v[4:5], v[14:17], off offset:-2048
	s_waitcnt vmcnt(11)
	v_lshlrev_b32_e32 v20, 16, v32
	v_and_b32_e32 v21, 0xffff0000, v32
	v_lshlrev_b32_e32 v22, 16, v48
	v_and_b32_e32 v23, 0xffff0000, v48
	v_lshlrev_b32_e32 v14, 16, v33
	v_and_b32_e32 v15, 0xffff0000, v33
	v_lshlrev_b32_e32 v16, 16, v49
	v_and_b32_e32 v17, 0xffff0000, v49
	v_lshlrev_b32_e32 v24, 16, v64
	v_and_b32_e32 v25, 0xffff0000, v64
	v_lshlrev_b32_e32 v18, 16, v65
	v_and_b32_e32 v19, 0xffff0000, v65
	v_pk_fma_f32 v[20:21], v[6:7], v[22:23], v[20:21] op_sel_hi:[0,1,1]
	v_pk_fma_f32 v[14:15], v[6:7], v[16:17], v[14:15] op_sel_hi:[0,1,1]
	v_pk_fma_f32 v[16:17], v[8:9], v[18:19], v[14:15] op_sel_hi:[0,1,1]
	v_pk_fma_f32 v[14:15], v[8:9], v[24:25], v[20:21] op_sel_hi:[0,1,1]
	global_store_dwordx4 v[4:5], v[14:17], off offset:-1024
	s_waitcnt vmcnt(10)
	v_lshlrev_b32_e32 v20, 16, v34
	v_and_b32_e32 v21, 0xffff0000, v34
	v_lshlrev_b32_e32 v22, 16, v50
	v_and_b32_e32 v23, 0xffff0000, v50
	v_lshlrev_b32_e32 v14, 16, v35
	v_and_b32_e32 v15, 0xffff0000, v35
	v_lshlrev_b32_e32 v16, 16, v51
	v_and_b32_e32 v17, 0xffff0000, v51
	v_lshlrev_b32_e32 v24, 16, v66
	v_and_b32_e32 v25, 0xffff0000, v66
	v_lshlrev_b32_e32 v18, 16, v67
	v_and_b32_e32 v19, 0xffff0000, v67
	v_pk_fma_f32 v[20:21], v[6:7], v[22:23], v[20:21] op_sel_hi:[0,1,1]
	v_pk_fma_f32 v[14:15], v[6:7], v[16:17], v[14:15] op_sel_hi:[0,1,1]
	v_pk_fma_f32 v[16:17], v[8:9], v[18:19], v[14:15] op_sel_hi:[0,1,1]
	v_pk_fma_f32 v[14:15], v[8:9], v[24:25], v[20:21] op_sel_hi:[0,1,1]
	global_store_dwordx4 v[4:5], v[14:17], off
	s_waitcnt vmcnt(9)
	v_lshlrev_b32_e32 v20, 16, v36
	v_and_b32_e32 v21, 0xffff0000, v36
	v_lshlrev_b32_e32 v22, 16, v52
	v_and_b32_e32 v23, 0xffff0000, v52
	v_lshlrev_b32_e32 v14, 16, v37
	v_and_b32_e32 v15, 0xffff0000, v37
	v_lshlrev_b32_e32 v16, 16, v53
	v_and_b32_e32 v17, 0xffff0000, v53
	v_lshlrev_b32_e32 v24, 16, v68
	v_and_b32_e32 v25, 0xffff0000, v68
	v_lshlrev_b32_e32 v18, 16, v69
	v_and_b32_e32 v19, 0xffff0000, v69
	v_pk_fma_f32 v[20:21], v[6:7], v[22:23], v[20:21] op_sel_hi:[0,1,1]
	v_pk_fma_f32 v[14:15], v[6:7], v[16:17], v[14:15] op_sel_hi:[0,1,1]
	v_pk_fma_f32 v[16:17], v[8:9], v[18:19], v[14:15] op_sel_hi:[0,1,1]
	v_pk_fma_f32 v[14:15], v[8:9], v[24:25], v[20:21] op_sel_hi:[0,1,1]
	global_store_dwordx4 v[4:5], v[14:17], off offset:1024
	s_waitcnt vmcnt(8)
	v_lshlrev_b32_e32 v20, 16, v38
	v_and_b32_e32 v21, 0xffff0000, v38
	v_lshlrev_b32_e32 v22, 16, v54
	v_and_b32_e32 v23, 0xffff0000, v54
	v_lshlrev_b32_e32 v14, 16, v39
	v_and_b32_e32 v15, 0xffff0000, v39
	v_lshlrev_b32_e32 v16, 16, v55
	v_and_b32_e32 v17, 0xffff0000, v55
	v_lshlrev_b32_e32 v24, 16, v70
	v_and_b32_e32 v25, 0xffff0000, v70
	v_lshlrev_b32_e32 v18, 16, v71
	v_and_b32_e32 v19, 0xffff0000, v71
	v_pk_fma_f32 v[20:21], v[6:7], v[22:23], v[20:21] op_sel_hi:[0,1,1]
	v_pk_fma_f32 v[14:15], v[6:7], v[16:17], v[14:15] op_sel_hi:[0,1,1]
	v_pk_fma_f32 v[16:17], v[8:9], v[18:19], v[14:15] op_sel_hi:[0,1,1]
	v_pk_fma_f32 v[14:15], v[8:9], v[24:25], v[20:21] op_sel_hi:[0,1,1]
	global_store_dwordx4 v[4:5], v[14:17], off offset:2048
	s_waitcnt vmcnt(7)
	v_lshlrev_b32_e32 v20, 16, v40
	v_and_b32_e32 v21, 0xffff0000, v40
	v_lshlrev_b32_e32 v22, 16, v56
	v_and_b32_e32 v23, 0xffff0000, v56
	v_lshlrev_b32_e32 v14, 16, v41
	v_and_b32_e32 v15, 0xffff0000, v41
	v_lshlrev_b32_e32 v16, 16, v57
	v_and_b32_e32 v17, 0xffff0000, v57
	v_lshlrev_b32_e32 v24, 16, v72
	v_and_b32_e32 v25, 0xffff0000, v72
	v_lshlrev_b32_e32 v18, 16, v73
	v_and_b32_e32 v19, 0xffff0000, v73
	v_pk_fma_f32 v[20:21], v[6:7], v[22:23], v[20:21] op_sel_hi:[0,1,1]
	v_pk_fma_f32 v[14:15], v[6:7], v[16:17], v[14:15] op_sel_hi:[0,1,1]
	v_pk_fma_f32 v[16:17], v[8:9], v[18:19], v[14:15] op_sel_hi:[0,1,1]
	v_pk_fma_f32 v[14:15], v[8:9], v[24:25], v[20:21] op_sel_hi:[0,1,1]
	global_store_dwordx4 v[4:5], v[14:17], off offset:3072
	v_lshl_add_u64 v[4:5], v[4:5], 0, s[12:13]
	s_cbranch_scc1 .LBB0_1885
